# prologue rmsnorm row loop: loop-invariant gain loads hoisted, next row prefetched, counted wait
# speedup vs baseline: 1.0150x; 1.0021x over previous
.LBB0_13:
	s_or_b64 exec, exec, s[4:5]
	v_mov_b32_e32 v1, v0
	v_readlane_b32 s0, v253, 63
	v_ashrrev_i32_e32 v3, 6, v1
	s_nop 0
	v_add_u32_e32 v4, s0, v3
	s_movk_i32 s0, 0x4000
	v_cmp_gt_i32_e32 vcc, s0, v4
	s_and_saveexec_b64 s[0:1], vcc
	v_readlane_b32 s16, v252, 0
	v_readlane_b32 s17, v252, 1
	s_cbranch_execz .LBB0_16
	v_and_b32_e32 v16, 63, v1
	v_mbcnt_lo_u32_b32 v1, -1, 0
	v_mbcnt_hi_u32_b32 v5, -1, v1
	v_and_b32_e32 v1, 64, v5
	v_add_u32_e32 v6, 64, v1
	v_xor_b32_e32 v1, 32, v5
	v_cmp_lt_i32_e32 vcc, v1, v6
	v_xor_b32_e32 v3, 16, v5
	v_xor_b32_e32 v7, 8, v5
	v_cndmask_b32_e32 v1, v5, v1, vcc
	v_cmp_lt_i32_e32 vcc, v3, v6
	v_lshlrev_b32_e32 v10, 4, v16
	v_readlane_b32 s52, v253, 2
	v_cndmask_b32_e32 v3, v5, v3, vcc
	v_cmp_lt_i32_e32 vcc, v7, v6
	v_mov_b32_e32 v11, 0
	v_readlane_b32 s53, v253, 3
	v_cndmask_b32_e32 v7, v5, v7, vcc
	v_lshlrev_b32_e32 v12, 2, v7
	v_xor_b32_e32 v7, 4, v5
	v_cmp_lt_i32_e32 vcc, v7, v6
	v_readlane_b32 s56, v253, 6
	v_readlane_b32 s57, v253, 7
	v_cndmask_b32_e32 v7, v5, v7, vcc
	v_lshlrev_b32_e32 v13, 2, v7
	v_xor_b32_e32 v7, 2, v5
	v_cmp_lt_i32_e32 vcc, v7, v6
	s_mov_b64 s[4:5], 0x4800000
	s_ashr_i32 s17, s16, 31
	v_cndmask_b32_e32 v7, v5, v7, vcc
	v_lshlrev_b32_e32 v14, 2, v7
	v_xor_b32_e32 v7, 1, v5
	v_cmp_lt_i32_e32 vcc, v7, v6
	s_mov_b64 s[6:7], 0x800
	v_lshlrev_b32_e32 v1, 2, v1
	v_cndmask_b32_e32 v5, v5, v7, vcc
	v_lshlrev_b32_e32 v15, 2, v5
	v_ashrrev_i32_e32 v5, 31, v4
	v_lshlrev_b64 v[8:9], 11, v[4:5]
	v_lshl_or_b32 v8, v16, 3, v8
	v_lshlrev_b64 v[16:17], 12, v[4:5]
	v_or_b32_e32 v16, v16, v10
	v_lshl_add_u64 v[6:7], s[56:57], 0, v[10:11]
	v_lshl_add_u64 v[8:9], s[48:49], 0, v[8:9]
	v_lshl_add_u64 v[10:11], s[52:53], 0, v[16:17]
	v_lshlrev_b32_e32 v3, 2, v3
	v_lshl_add_u64 v[8:9], v[8:9], 0, s[4:5]
	s_lshl_b64 s[4:5], s[16:17], 11
	v_lshl_add_u64 v[10:11], v[10:11], 0, s[6:7]
	s_lshl_b64 s[6:7], s[16:17], 12
	s_mov_b64 s[8:9], 0
	v_mov_b32_e32 v5, 0x358637bd
	s_movk_i32 s14, 0x3fff
	s_mov_b32 s15, 0x800000
	v_readlane_b32 s54, v253, 4
	v_readlane_b32 s55, v253, 5
	v_readlane_b32 s58, v253, 8
	v_readlane_b32 s59, v253, 9
	v_readlane_b32 s60, v253, 10
	v_readlane_b32 s61, v253, 11
	v_readlane_b32 s62, v253, 12
	v_readlane_b32 s63, v253, 13
	v_readlane_b32 s64, v253, 14
	v_readlane_b32 s65, v253, 15
	v_readlane_b32 s66, v253, 16
	v_readlane_b32 s67, v253, 17
	global_load_dwordx4 v[54:57], v[6:7], off
	global_load_dwordx4 v[58:61], v[6:7], off offset:1024
	global_load_dwordx4 v[62:65], v[6:7], off offset:2048
	global_load_dwordx4 v[66:69], v[6:7], off offset:3072
	global_load_dwordx4 v[70:73], v[10:11], off offset:-2048
	global_load_dwordx4 v[74:77], v[10:11], off offset:-1024
	global_load_dwordx4 v[78:81], v[10:11], off
	global_load_dwordx4 v[82:85], v[10:11], off offset:1024
	s_waitcnt vmcnt(0)
.LBB0_15:
	s_waitcnt vmcnt(4)
	v_mov_b64_e32 v[16:17], v[70:71]
	v_mov_b64_e32 v[18:19], v[72:73]
	v_mov_b64_e32 v[20:21], v[74:75]
	v_mov_b64_e32 v[22:23], v[76:77]
	v_mov_b64_e32 v[24:25], v[78:79]
	v_mov_b64_e32 v[26:27], v[80:81]
	v_mov_b64_e32 v[28:29], v[82:83]
	v_mov_b64_e32 v[30:31], v[84:85]
	v_add_u32_e32 v4, s16, v4
	v_lshl_add_u64 v[10:11], v[10:11], 0, s[6:7]
	v_cmp_lt_i32_e32 vcc, s14, v4
	s_or_b64 s[8:9], vcc, s[8:9]
	s_cbranch_vccnz .Lrms_nopf
	global_load_dwordx4 v[70:73], v[10:11], off offset:-2048
	global_load_dwordx4 v[74:77], v[10:11], off offset:-1024
	global_load_dwordx4 v[78:81], v[10:11], off
	global_load_dwordx4 v[82:85], v[10:11], off offset:1024
.Lrms_nopf:
	v_mov_b32_e32 v42, v17
	v_mov_b32_e32 v43, v21
	v_mov_b32_e32 v40, v16
	v_mov_b32_e32 v41, v20
	v_mov_b32_e32 v50, v25
	v_mov_b32_e32 v51, v29
	v_pk_mul_f32 v[42:43], v[42:43], v[42:43]
	v_mov_b32_e32 v36, v18
	v_mov_b32_e32 v37, v22
	v_mov_b32_e32 v48, v24
	v_mov_b32_e32 v49, v28
	v_pk_mul_f32 v[50:51], v[50:51], v[50:51]
	v_pk_fma_f32 v[40:41], v[40:41], v[40:41], v[42:43]
	v_mov_b32_e32 v38, v19
	v_mov_b32_e32 v39, v23
	v_mov_b32_e32 v44, v26
	v_mov_b32_e32 v45, v30
	v_pk_fma_f32 v[42:43], v[48:49], v[48:49], v[50:51]
	v_pk_fma_f32 v[36:37], v[36:37], v[36:37], v[40:41]
	v_mov_b32_e32 v46, v27
	v_mov_b32_e32 v47, v31
	v_pk_fma_f32 v[40:41], v[44:45], v[44:45], v[42:43]
	v_pk_fma_f32 v[36:37], v[38:39], v[38:39], v[36:37]
	v_pk_fma_f32 v[38:39], v[46:47], v[46:47], v[40:41]
	v_add_f32_e32 v36, v36, v37
	v_add_f32_e32 v36, v36, v38
	v_add_f32_e32 v36, v36, v39
	ds_bpermute_b32 v37, v1, v36
	s_waitcnt lgkmcnt(0)
	v_add_f32_e32 v36, v36, v37
	ds_bpermute_b32 v37, v3, v36
	s_waitcnt lgkmcnt(0)
	v_add_f32_e32 v36, v36, v37
	ds_bpermute_b32 v37, v12, v36
	s_waitcnt lgkmcnt(0)
	v_add_f32_e32 v36, v36, v37
	ds_bpermute_b32 v37, v13, v36
	s_waitcnt lgkmcnt(0)
	v_add_f32_e32 v36, v36, v37
	ds_bpermute_b32 v37, v14, v36
	s_waitcnt lgkmcnt(0)
	v_add_f32_e32 v36, v36, v37
	ds_bpermute_b32 v37, v15, v36
	s_waitcnt lgkmcnt(0)
	v_add_f32_e32 v36, v36, v37
	v_fmamk_f32 v36, v36, 0x3a800000, v5
	v_mul_f32_e32 v37, 0x4b800000, v36
	v_cmp_gt_f32_e32 vcc, s15, v36
	s_nop 1
	v_cndmask_b32_e32 v36, v36, v37, vcc
	v_rsq_f32_e32 v36, v36
	s_nop 0
	v_mul_f32_e32 v37, 0x45800000, v36
	v_cndmask_b32_e32 v36, v36, v37, vcc
	v_pk_mul_f32 v[16:17], v[16:17], v[36:37] op_sel_hi:[1,0]
	v_pk_mul_f32 v[18:19], v[18:19], v[36:37] op_sel_hi:[1,0]
	v_pk_mul_f32 v[16:17], v[54:55], v[16:17]
	v_pk_mul_f32 v[18:19], v[56:57], v[18:19]
	v_cvt_pk_bf16_f32 v86, v16, v17
	v_cvt_pk_bf16_f32 v87, v18, v19
	global_store_dwordx2 v[8:9], v[86:87], off
	v_pk_mul_f32 v[20:21], v[20:21], v[36:37] op_sel_hi:[1,0]
	v_pk_mul_f32 v[22:23], v[22:23], v[36:37] op_sel_hi:[1,0]
	v_pk_mul_f32 v[16:17], v[58:59], v[20:21]
	v_pk_mul_f32 v[18:19], v[60:61], v[22:23]
	v_cvt_pk_bf16_f32 v88, v16, v17
	v_cvt_pk_bf16_f32 v89, v18, v19
	global_store_dwordx2 v[8:9], v[88:89], off offset:512
	v_pk_mul_f32 v[20:21], v[24:25], v[36:37] op_sel_hi:[1,0]
	v_pk_mul_f32 v[22:23], v[26:27], v[36:37] op_sel_hi:[1,0]
	v_pk_mul_f32 v[16:17], v[62:63], v[20:21]
	v_pk_mul_f32 v[18:19], v[22:23], v[64:65]
	v_cvt_pk_bf16_f32 v90, v16, v17
	v_cvt_pk_bf16_f32 v91, v18, v19
	global_store_dwordx2 v[8:9], v[90:91], off offset:1024
	v_pk_mul_f32 v[20:21], v[28:29], v[36:37] op_sel_hi:[1,0]
	v_pk_mul_f32 v[22:23], v[30:31], v[36:37] op_sel_hi:[1,0]
	v_pk_mul_f32 v[16:17], v[20:21], v[66:67]
	v_pk_mul_f32 v[18:19], v[22:23], v[68:69]
	v_cvt_pk_bf16_f32 v92, v16, v17
	v_cvt_pk_bf16_f32 v93, v18, v19
	global_store_dwordx2 v[8:9], v[92:93], off offset:1536
	v_lshl_add_u64 v[8:9], v[8:9], 0, s[4:5]
	s_andn2_b64 exec, exec, s[8:9]
	s_cbranch_execnz .LBB0_15
